# DPP/permlane-swap reductions replace ds_bpermute butterflies in the three row-norm loops (P1 norm, P6 dense, P6 MoE)
# speedup vs baseline: 1.0085x; 1.0085x over previous
.LBB0_72:
	s_waitcnt lgkmcnt(0)
	v_pk_mul_f32 v[182:183], v[20:21], v[20:21]
	v_pk_mul_f32 v[184:185], v[18:19], v[18:19]
	v_pk_mul_f32 v[178:179], v[24:25], v[24:25]
	v_pk_mul_f32 v[180:181], v[22:23], v[22:23]
	v_pk_mov_b32 v[186:187], v[184:185], v[182:183] op_sel:[1,0]
	v_mov_b32_e32 v185, v183
	v_pk_add_f32 v[182:183], v[186:187], v[184:185]
	v_pk_mov_b32 v[184:185], v[180:181], v[178:179] op_sel:[1,0]
	v_mov_b32_e32 v181, v179
	v_pk_add_f32 v[178:179], v[184:185], v[180:181]
	v_pk_add_f32 v[182:183], v[182:183], v[182:183] op_sel_hi:[0,1]
	v_pk_add_f32 v[178:179], v[178:179], v[178:179] op_sel_hi:[0,1]
	v_mul_f32_e32 v178, v26, v26
	v_pk_fma_f32 v[180:181], v[26:27], v[26:27], v[178:179] op_sel_hi:[1,1,0]
	v_mul_f32_e32 v178, v28, v28
	v_pk_fma_f32 v[184:185], v[28:29], v[28:29], v[178:179] op_sel_hi:[1,1,0]
	v_mul_f32_e32 v180, v30, v30
	v_mul_f32_e32 v184, v31, v31
	v_mul_f32_e32 v182, v32, v32
	v_mul_f32_e32 v178, v33, v33
	v_pk_add_f32 v[180:181], v[180:181], v[184:185]
	v_pk_add_f32 v[178:179], v[182:183], v[178:179]
	s_nop 0
	v_pk_add_f32 v[178:179], v[180:181], v[178:179]
	s_nop 0
	v_add_f32_e32 v178, v178, v179
	s_nop 1
	v_add_f32_dpp v178, v178, v178 quad_perm:[1,0,3,2] row_mask:0xf bank_mask:0xf
	s_nop 1
	v_add_f32_dpp v178, v178, v178 quad_perm:[2,3,0,1] row_mask:0xf bank_mask:0xf
	s_nop 1
	v_add_f32_dpp v178, v178, v178 row_half_mirror row_mask:0xf bank_mask:0xf
	s_nop 1
	v_add_f32_dpp v178, v178, v178 row_ror:8 row_mask:0xf bank_mask:0xf
	v_mov_b32_e32 v179, v178
	s_nop 1
	v_permlane16_swap_b32_e32 v178, v179
	s_nop 0
	v_add_f32_e32 v178, v178, v179
	v_mov_b32_e32 v179, v178
	s_nop 1
	v_permlane32_swap_b32_e32 v178, v179
	s_nop 0
	v_add_f32_e32 v178, v178, v179
	v_fmamk_f32 v178, v178, 0x3a800000, v235
	v_rsq_f32_e32 v182, v178
	s_nop 0
	v_pk_mul_f32 v[18:19], v[18:19], v[182:183] op_sel_hi:[1,0]
	v_pk_mul_f32 v[20:21], v[20:21], v[182:183] op_sel_hi:[1,0]
	v_pk_mul_f32 v[22:23], v[22:23], v[182:183] op_sel_hi:[1,0]
	v_pk_mul_f32 v[24:25], v[24:25], v[182:183] op_sel_hi:[1,0]
	s_waitcnt vmcnt(35)
	v_pk_mul_f32 v[178:179], v[36:37], v[20:21]
	v_pk_mul_f32 v[180:181], v[34:35], v[18:19]
	v_pk_mul_f32 v[18:19], v[32:33], v[182:183] op_sel_hi:[1,0]
	v_pk_mul_f32 v[26:27], v[26:27], v[182:183] op_sel_hi:[1,0]
	v_pk_mul_f32 v[184:185], v[28:29], v[182:183] op_sel_hi:[1,0]
	v_pk_mul_f32 v[186:187], v[30:31], v[182:183] op_sel_hi:[1,0]
	s_waitcnt vmcnt(34)
	v_pk_mul_f32 v[28:29], v[40:41], v[24:25]
	v_pk_mul_f32 v[30:31], v[38:39], v[22:23]
	s_waitcnt vmcnt(32)
	v_pk_mul_f32 v[22:23], v[48:49], v[18:19]
	v_max_f32_e64 v18, |v180|, |v181|
	v_max_f32_e64 v19, |v178|, |v179|
	v_pk_mul_f32 v[20:21], v[44:45], v[184:185]
	v_pk_mul_f32 v[24:25], v[42:43], v[26:27]
	v_max3_f32 v18, v18, 0, v19
	v_max_f32_e64 v19, |v30|, |v31|
	v_max_f32_e64 v32, |v28|, |v29|
	v_pk_mul_f32 v[26:27], v[46:47], v[186:187]
	v_max3_f32 v18, v18, v19, v32
	v_max_f32_e64 v19, |v24|, |v25|
	v_max_f32_e64 v32, |v20|, |v21|
	v_max3_f32 v18, v18, v19, v32
	v_max_f32_e64 v19, |v26|, |v27|
	v_max_f32_e64 v32, |v22|, |v23|
	v_max3_f32 v18, v18, v19, v32
	s_nop 1
	v_max_f32_dpp v18, v18, v18 quad_perm:[1,0,3,2] row_mask:0xf bank_mask:0xf
	s_nop 1
	v_max_f32_dpp v18, v18, v18 quad_perm:[2,3,0,1] row_mask:0xf bank_mask:0xf
	s_nop 1
	v_max_f32_dpp v18, v18, v18 row_half_mirror row_mask:0xf bank_mask:0xf
	s_nop 1
	v_max_f32_dpp v18, v18, v18 row_ror:8 row_mask:0xf bank_mask:0xf
	v_mov_b32_e32 v19, v18
	s_nop 1
	v_permlane16_swap_b32_e32 v18, v19
	s_nop 0
	v_max_f32_e32 v18, v18, v19
	v_mov_b32_e32 v19, v18
	s_nop 1
	v_permlane32_swap_b32_e32 v18, v19
	s_nop 0
	v_max_f32_e32 v18, v18, v19
	s_and_saveexec_b64 s[4:5], s[6:7]
	s_xor_b64 s[16:17], exec, s[4:5]
	s_add_u32 s38, s50, s20
	s_addc_u32 s39, s51, s21
	s_or_saveexec_b64 s[16:17], s[16:17]
	s_waitcnt lgkmcnt(0)
	v_max_f32_e32 v32, s72, v18
	v_mov_b64_e32 v[18:19], s[38:39]
	s_xor_b64 exec, exec, s[16:17]
	s_cbranch_execz .LBB0_76
	v_mul_f32_e32 v18, 0x3c010204, v32
	s_ashr_i32 s37, s36, 31
	global_store_dword v1, v18, s[26:27]
	v_mov_b64_e32 v[18:19], s[36:37]
.LBB0_76:
	s_or_b64 exec, exec, s[16:17]
	v_div_scale_f32 v33, s[4:5], v32, v32, s73
	v_rcp_f32_e32 v182, v33
	s_nop 0
	v_fma_f32 v183, -v33, v182, 1.0
	v_fmac_f32_e32 v182, v183, v182
	v_div_scale_f32 v183, vcc, s73, v32, s73
	v_mul_f32_e32 v184, v183, v182
	v_fma_f32 v185, -v33, v184, v183
	v_fmac_f32_e32 v184, v185, v182
	v_fma_f32 v33, -v33, v184, v183
	v_div_fmas_f32 v33, v33, v182, v184
	v_div_fixup_f32 v182, v33, v32, s73
	v_mul_f32_e32 v184, v181, v182
	v_mul_f32_e32 v185, v178, v182
	v_mul_f32_e32 v183, v180, v182
	v_mul_f32_e32 v186, v179, v182
	v_rndne_f32_e32 v184, v184
	v_rndne_f32_e32 v185, v185
	v_rndne_f32_e32 v183, v183
	v_cvt_i32_f32_e32 v184, v184
	v_cvt_i32_f32_e32 v185, v185
	v_rndne_f32_e32 v186, v186
	v_cvt_i32_f32_e32 v183, v183
	v_cvt_i32_f32_e32 v186, v186
	v_med3_i32 v184, v184, s84, v236
	v_med3_i32 v185, v185, s84, v236
	v_med3_i32 v183, v183, s84, v236
	v_med3_i32 v186, v186, s84, v236
	v_lshlrev_b32_e32 v184, 8, v184
	v_lshlrev_b32_e32 v185, 16, v185
	v_lshlrev_b64 v[32:33], 10, v[18:19]
	v_and_b32_e32 v184, 0xff00, v184
	v_and_b32_e32 v185, 0xff0000, v185
	v_perm_b32 v183, v186, v183, s60
	v_or3_b32 v183, v183, v184, v185
	v_lshl_add_u64 v[32:33], v[210:211], 0, v[32:33]
	v_mul_f32_e32 v184, v31, v182
	v_mul_f32_e32 v185, v28, v182
	global_store_dword v[32:33], v183, off
	v_mul_f32_e32 v183, v30, v182
	v_mul_f32_e32 v186, v29, v182
	v_rndne_f32_e32 v184, v184
	v_rndne_f32_e32 v185, v185
	v_rndne_f32_e32 v183, v183
	v_cvt_i32_f32_e32 v184, v184
	v_cvt_i32_f32_e32 v185, v185
	v_rndne_f32_e32 v186, v186
	v_cvt_i32_f32_e32 v183, v183
	v_cvt_i32_f32_e32 v186, v186
	v_med3_i32 v184, v184, s84, v236
	v_med3_i32 v185, v185, s84, v236
	v_med3_i32 v183, v183, s84, v236
	v_med3_i32 v186, v186, s84, v236
	v_lshlrev_b32_e32 v184, 8, v184
	v_lshlrev_b32_e32 v185, 16, v185
	v_and_b32_e32 v184, 0xff00, v184
	v_and_b32_e32 v185, 0xff0000, v185
	v_perm_b32 v183, v186, v183, s60
	v_or3_b32 v183, v183, v184, v185
	v_mul_f32_e32 v184, v25, v182
	v_mul_f32_e32 v185, v20, v182
	global_store_dword v[32:33], v183, off offset:256
	v_mul_f32_e32 v183, v24, v182
	v_mul_f32_e32 v186, v21, v182
	v_rndne_f32_e32 v184, v184
	v_rndne_f32_e32 v185, v185
	v_rndne_f32_e32 v183, v183
	v_cvt_i32_f32_e32 v184, v184
	v_cvt_i32_f32_e32 v185, v185
	v_rndne_f32_e32 v186, v186
	v_cvt_i32_f32_e32 v183, v183
	v_cvt_i32_f32_e32 v186, v186
	v_med3_i32 v184, v184, s84, v236
	v_med3_i32 v185, v185, s84, v236
	v_med3_i32 v183, v183, s84, v236
	v_med3_i32 v186, v186, s84, v236
	v_lshlrev_b32_e32 v184, 8, v184
	v_lshlrev_b32_e32 v185, 16, v185
	v_and_b32_e32 v184, 0xff00, v184
	v_and_b32_e32 v185, 0xff0000, v185
	v_perm_b32 v183, v186, v183, s60
	v_or3_b32 v183, v183, v184, v185
	v_mul_f32_e32 v184, v27, v182
	v_mul_f32_e32 v185, v22, v182
	global_store_dword v[32:33], v183, off offset:512
	v_mul_f32_e32 v183, v26, v182
	v_mul_f32_e32 v182, v23, v182
	v_rndne_f32_e32 v184, v184
	v_rndne_f32_e32 v185, v185
	v_rndne_f32_e32 v183, v183
	v_cvt_i32_f32_e32 v184, v184
	v_cvt_i32_f32_e32 v185, v185
	v_rndne_f32_e32 v182, v182
	v_cvt_i32_f32_e32 v183, v183
	v_cvt_i32_f32_e32 v182, v182
	v_med3_i32 v184, v184, s84, v236
	v_med3_i32 v185, v185, s84, v236
	v_med3_i32 v183, v183, s84, v236
	v_med3_i32 v182, v182, s84, v236
	v_lshlrev_b32_e32 v184, 8, v184
	v_lshlrev_b32_e32 v185, 16, v185
	v_and_b32_e32 v184, 0xff00, v184
	v_and_b32_e32 v185, 0xff0000, v185
	v_perm_b32 v182, v182, v183, s60
	v_or3_b32 v182, v182, v184, v185
	global_store_dword v[32:33], v182, off offset:768
	s_waitcnt vmcnt(35)
	v_fma_f32 v32, v50, v180, 0
	s_waitcnt vmcnt(33)
	v_fma_f32 v184, v58, v180, 0
	v_fmac_f32_e32 v32, v54, v181
	v_fma_f32 v33, v51, v180, 0
	s_waitcnt vmcnt(32)
	v_fmac_f32_e32 v184, v62, v181
	v_fma_f32 v185, v59, v180, 0
	s_waitcnt vmcnt(31)
	v_fmac_f32_e32 v32, v66, v178
	v_fmac_f32_e32 v33, v55, v181
	v_fma_f32 v182, v52, v180, 0
	s_waitcnt vmcnt(29)
	v_fmac_f32_e32 v184, v74, v178
	v_fmac_f32_e32 v185, v63, v181
	v_fma_f32 v186, v60, v180, 0
	v_fmac_f32_e32 v32, v70, v179
	v_fmac_f32_e32 v33, v67, v178
	v_fmac_f32_e32 v182, v56, v181
	v_fma_f32 v183, v53, v180, 0
	s_waitcnt vmcnt(28)
	v_fmac_f32_e32 v184, v78, v179
	v_fmac_f32_e32 v185, v75, v178
	v_fmac_f32_e32 v186, v64, v181
	v_fma_f32 v180, v61, v180, 0
	s_waitcnt vmcnt(27)
	v_fmac_f32_e32 v32, v82, v30
	v_fmac_f32_e32 v33, v71, v179
	v_fmac_f32_e32 v182, v68, v178
	v_fmac_f32_e32 v183, v57, v181
	s_waitcnt vmcnt(25)
	v_fmac_f32_e32 v184, v90, v30
	v_fmac_f32_e32 v185, v79, v179
	v_fmac_f32_e32 v186, v76, v178
	v_fmac_f32_e32 v180, v65, v181
	v_fmac_f32_e32 v32, v86, v31
	v_fmac_f32_e32 v33, v83, v30
	v_fmac_f32_e32 v182, v72, v179
	v_fmac_f32_e32 v183, v69, v178
	s_waitcnt vmcnt(24)
	v_fmac_f32_e32 v184, v94, v31
	v_fmac_f32_e32 v185, v91, v30
	v_fmac_f32_e32 v186, v80, v179
	v_fmac_f32_e32 v180, v77, v178
	s_waitcnt vmcnt(23)
	v_fmac_f32_e32 v32, v98, v28
	v_fmac_f32_e32 v33, v87, v31
	v_fmac_f32_e32 v182, v84, v30
	v_fmac_f32_e32 v183, v73, v179
	s_waitcnt vmcnt(21)
	v_fmac_f32_e32 v184, v106, v28
	v_fmac_f32_e32 v185, v95, v31
	v_fmac_f32_e32 v186, v92, v30
	v_fmac_f32_e32 v180, v81, v179
	v_fmac_f32_e32 v32, v102, v29
	v_fmac_f32_e32 v33, v99, v28
	v_fmac_f32_e32 v182, v88, v31
	v_fmac_f32_e32 v183, v85, v30
	s_waitcnt vmcnt(20)
	v_fmac_f32_e32 v184, v110, v29
	v_fmac_f32_e32 v185, v107, v28
	v_fmac_f32_e32 v186, v96, v31
	v_fmac_f32_e32 v180, v93, v30
	s_waitcnt vmcnt(19)
	v_fmac_f32_e32 v32, v114, v24
	v_fmac_f32_e32 v33, v103, v29
	v_fmac_f32_e32 v182, v100, v28
	v_fmac_f32_e32 v183, v89, v31
	s_waitcnt vmcnt(17)
	v_fmac_f32_e32 v184, v122, v24
	v_fmac_f32_e32 v185, v111, v29
	v_fmac_f32_e32 v186, v108, v28
	v_fmac_f32_e32 v180, v97, v31
	v_fmac_f32_e32 v32, v118, v25
	v_fmac_f32_e32 v33, v115, v24
	v_fmac_f32_e32 v182, v104, v29
	v_fmac_f32_e32 v183, v101, v28
	s_waitcnt vmcnt(16)
	v_fmac_f32_e32 v184, v126, v25
	v_fmac_f32_e32 v185, v123, v24
	v_fmac_f32_e32 v186, v112, v29
	v_fmac_f32_e32 v180, v109, v28
	s_waitcnt vmcnt(15)
	v_fmac_f32_e32 v32, v130, v20
	v_fmac_f32_e32 v33, v119, v25
	v_fmac_f32_e32 v182, v116, v24
	v_fmac_f32_e32 v183, v105, v29
	s_waitcnt vmcnt(13)
	v_fmac_f32_e32 v184, v138, v20
	v_fmac_f32_e32 v185, v127, v25
	v_fmac_f32_e32 v186, v124, v24
	v_fmac_f32_e32 v180, v113, v29
	v_fmac_f32_e32 v32, v134, v21
	v_fmac_f32_e32 v33, v131, v20
	v_fmac_f32_e32 v182, v120, v25
	v_fmac_f32_e32 v183, v117, v24
	s_waitcnt vmcnt(12)
	v_fmac_f32_e32 v184, v142, v21
	v_fmac_f32_e32 v185, v139, v20
	v_fmac_f32_e32 v186, v128, v25
	v_fmac_f32_e32 v180, v125, v24
	s_waitcnt vmcnt(11)
	v_fmac_f32_e32 v32, v146, v26
	v_fmac_f32_e32 v33, v135, v21
	v_fmac_f32_e32 v182, v132, v20
	v_fmac_f32_e32 v183, v121, v25
	s_waitcnt vmcnt(9)
	v_fmac_f32_e32 v184, v154, v26
	v_fmac_f32_e32 v185, v143, v21
	v_fmac_f32_e32 v186, v140, v20
	v_fmac_f32_e32 v180, v129, v25
	v_fmac_f32_e32 v32, v150, v27
	v_fmac_f32_e32 v33, v147, v26
	v_fmac_f32_e32 v182, v136, v21
	v_fmac_f32_e32 v183, v133, v20
	s_waitcnt vmcnt(8)
	v_fmac_f32_e32 v184, v158, v27
	v_fmac_f32_e32 v185, v155, v26
	v_fmac_f32_e32 v186, v144, v21
	v_fmac_f32_e32 v180, v141, v20
	s_waitcnt vmcnt(7)
	v_fmac_f32_e32 v32, v162, v22
	v_fmac_f32_e32 v33, v151, v27
	v_fmac_f32_e32 v182, v148, v26
	v_fmac_f32_e32 v183, v137, v21
	s_waitcnt vmcnt(5)
	v_fmac_f32_e32 v184, v170, v22
	v_fmac_f32_e32 v185, v159, v27
	v_fmac_f32_e32 v186, v156, v26
	v_fmac_f32_e32 v180, v145, v21
	v_fmac_f32_e32 v32, v166, v23
	v_fmac_f32_e32 v33, v163, v22
	v_fmac_f32_e32 v182, v152, v27
	v_fmac_f32_e32 v183, v149, v26
	s_waitcnt vmcnt(4)
	v_fmac_f32_e32 v184, v174, v23
	v_fmac_f32_e32 v185, v171, v22
	v_fmac_f32_e32 v186, v160, v27
	v_fmac_f32_e32 v180, v157, v26
	v_fmac_f32_e32 v33, v167, v23
	v_fmac_f32_e32 v182, v164, v22
	v_fmac_f32_e32 v183, v153, v27
	v_fmac_f32_e32 v185, v175, v23
	v_fmac_f32_e32 v186, v172, v22
	v_fmac_f32_e32 v180, v161, v27
	v_cndmask_b32_e64 v21, v32, v184, s[8:9]
	v_fmac_f32_e32 v182, v168, v23
	v_fmac_f32_e32 v183, v165, v22
	v_fmac_f32_e32 v186, v176, v23
	v_fmac_f32_e32 v180, v173, v22
	v_cndmask_b32_e64 v22, v33, v185, s[8:9]
	v_fmac_f32_e32 v183, v169, v23
	v_fmac_f32_e32 v180, v177, v23
	v_cndmask_b32_e64 v23, v182, v186, s[8:9]
	v_cndmask_b32_e64 v24, v183, v180, s[8:9]
	v_cndmask_b32_e64 v20, v184, v32, s[8:9]
	s_nop 1
	v_add_f32_dpp v20, v21, v20 row_shl:4 row_mask:0xf bank_mask:0x5
	s_nop 1
	v_add_f32_dpp v20, v21, v20 row_shr:4 row_mask:0xf bank_mask:0xa
	v_cndmask_b32_e64 v21, v185, v33, s[8:9]
	s_nop 1
	v_add_f32_dpp v21, v22, v21 row_shl:4 row_mask:0xf bank_mask:0x5
	s_nop 1
	v_add_f32_dpp v21, v22, v21 row_shr:4 row_mask:0xf bank_mask:0xa
	v_cndmask_b32_e64 v22, v186, v182, s[8:9]
	s_nop 1
	v_add_f32_dpp v22, v23, v22 row_shl:4 row_mask:0xf bank_mask:0x5
	s_nop 1
	v_add_f32_dpp v22, v23, v22 row_shr:4 row_mask:0xf bank_mask:0xa
	v_cndmask_b32_e64 v23, v180, v183, s[8:9]
	s_nop 1
	v_add_f32_dpp v23, v24, v23 row_shl:4 row_mask:0xf bank_mask:0x5
	s_nop 1
	v_add_f32_dpp v23, v24, v23 row_shr:4 row_mask:0xf bank_mask:0xa
	v_cndmask_b32_e64 v24, v22, v20, s[10:11]
	v_cndmask_b32_e64 v20, v20, v22, s[10:11]
	v_cndmask_b32_e64 v22, v23, v21, s[10:11]
	v_cndmask_b32_e64 v21, v21, v23, s[10:11]
	s_nop 1
	v_add_f32_dpp v20, v20, v24 quad_perm:[2,3,0,1] row_mask:0xf bank_mask:0xf
	v_add_f32_dpp v21, v21, v22 quad_perm:[2,3,0,1] row_mask:0xf bank_mask:0xf
	v_cndmask_b32_e64 v22, v21, v20, s[12:13]
	v_cndmask_b32_e64 v20, v20, v21, s[12:13]
	s_nop 1
	v_add_f32_dpp v20, v20, v22 quad_perm:[1,0,3,2] row_mask:0xf bank_mask:0xf
	s_nop 1
	v_add_f32_dpp v20, v20, v20 row_ror:8 row_mask:0xf bank_mask:0xf
	v_mov_b32_e32 v21, v20
	s_nop 1
	v_permlane16_swap_b32_e32 v20, v21
	s_nop 0
	v_add_f32_e32 v20, v20, v21
	v_mov_b32_e32 v21, v20
	s_nop 1
	v_permlane32_swap_b32_e32 v20, v21
	s_nop 0
	s_and_saveexec_b64 s[16:17], s[14:15]
	s_cbranch_execz .LBB0_59
	s_waitcnt lgkmcnt(0)
	v_add_f32_e32 v20, v20, v21
	global_load_dword v21, v[206:207], off
	v_lshlrev_b64 v[18:19], 5, v[18:19]
	v_lshl_add_u64 v[18:19], v[208:209], 0, v[18:19]
	s_waitcnt vmcnt(0)
	v_add_f32_e32 v20, v20, v21
	v_min_f32_e32 v21, 0, v20
	v_mul_f32_e64 v20, |v20|, s66
	v_exp_f32_e32 v20, v20
	s_nop 0
	v_add_f32_e32 v20, 1.0, v20
	v_log_f32_e32 v20, v20
	s_nop 0
	v_fmac_f32_e32 v21, 0xbf317218, v20
	global_store_dword v[18:19], v21, off
	s_branch .LBB0_59

.LBB0_951:
	v_lshlrev_b32_e32 v172, 16, v170
	v_and_b32_e32 v173, 0xffff0000, v170
	v_lshlrev_b32_e32 v170, 16, v171
	v_and_b32_e32 v171, 0xffff0000, v171
	v_lshlrev_b32_e32 v175, 16, v169
	v_lshlrev_b32_e32 v174, 16, v168
	v_and_b32_e32 v169, 0xffff0000, v169
	v_and_b32_e32 v168, 0xffff0000, v168
	v_lshlrev_b32_e32 v181, 16, v164
	v_and_b32_e32 v195, 0xffff0000, v164
	v_mul_f32_e32 v164, v171, v171
	v_mul_f32_e32 v180, v173, v173
	v_lshlrev_b32_e32 v196, 16, v165
	v_and_b32_e32 v197, 0xffff0000, v165
	v_pk_fma_f32 v[164:165], v[170:171], v[170:171], v[164:165] op_sel_hi:[1,1,0]
	v_pk_mul_f32 v[176:177], v[168:169], v[168:169]
	v_pk_fma_f32 v[204:205], v[172:173], v[172:173], v[180:181] op_sel_hi:[1,1,0]
	v_pk_fma_f32 v[176:177], v[174:175], v[174:175], v[176:177]
	v_mov_b32_e32 v180, v204
	v_mov_b32_e32 v206, v164
	v_mov_b32_e32 v207, v181
	v_mul_f32_e32 v194, v195, v195
	v_pk_add_f32 v[164:165], v[204:205], v[164:165]
	v_pk_mul_f32 v[204:205], v[180:181], v[206:207]
	v_pk_add_f32 v[176:177], v[176:177], v[176:177] op_sel:[0,1] op_sel_hi:[1,0]
	v_lshlrev_b32_e32 v178, 16, v166
	v_and_b32_e32 v179, 0xffff0000, v166
	v_lshlrev_b32_e32 v166, 16, v167
	v_and_b32_e32 v167, 0xffff0000, v167
	v_mov_b32_e32 v165, v205
	v_mov_b32_e32 v177, v194
	v_pk_add_f32 v[164:165], v[164:165], v[176:177]
	v_mul_f32_e32 v176, v179, v179
	v_mul_f32_e32 v180, v167, v167
	v_mul_f32_e32 v208, v196, v196
	v_mul_f32_e32 v209, v197, v197
	v_pk_fma_f32 v[176:177], v[178:179], v[178:179], v[176:177] op_sel_hi:[1,1,0]
	v_pk_fma_f32 v[204:205], v[166:167], v[166:167], v[180:181] op_sel_hi:[1,1,0]
	v_mov_b32_e32 v177, v208
	v_mov_b32_e32 v205, v209
	v_pk_add_f32 v[176:177], v[176:177], v[204:205]
	v_mov_b32_e32 v194, v181
	v_pk_add_f32 v[164:165], v[164:165], v[176:177]
	s_nop 0
	v_add_f32_e32 v164, v164, v165
	s_nop 1
	v_add_f32_dpp v164, v164, v164 quad_perm:[1,0,3,2] row_mask:0xf bank_mask:0xf
	s_nop 1
	v_add_f32_dpp v164, v164, v164 quad_perm:[2,3,0,1] row_mask:0xf bank_mask:0xf
	s_nop 1
	v_add_f32_dpp v164, v164, v164 row_half_mirror row_mask:0xf bank_mask:0xf
	s_nop 1
	v_add_f32_dpp v164, v164, v164 row_ror:8 row_mask:0xf bank_mask:0xf
	v_mov_b32_e32 v165, v164
	s_nop 1
	v_permlane16_swap_b32_e32 v164, v165
	s_nop 0
	v_add_f32_e32 v164, v164, v165
	v_mov_b32_e32 v165, v164
	s_nop 1
	v_permlane32_swap_b32_e32 v164, v165
	s_nop 0
	v_add_f32_e32 v164, v164, v165
	v_fmamk_f32 v164, v164, 0x3a800000, v235
	v_rsq_f32_e32 v180, v164
	s_nop 0
	v_pk_mul_f32 v[172:173], v[180:181], v[172:173] op_sel_hi:[0,1]
	v_pk_mul_f32 v[164:165], v[180:181], v[170:171] op_sel_hi:[0,1]
	v_pk_mul_f32 v[170:171], v[2:3], v[172:173]
	v_mov_b32_e32 v172, v174
	v_mov_b32_e32 v173, v168
	v_mov_b32_e32 v168, v175
	v_pk_mul_f32 v[164:165], v[4:5], v[164:165]
	v_pk_mul_f32 v[172:173], v[180:181], v[172:173] op_sel_hi:[0,1]
	v_pk_mul_f32 v[168:169], v[180:181], v[168:169] op_sel_hi:[0,1]
	v_pk_mul_f32 v[168:169], v[8:9], v[168:169]
	v_pk_mul_f32 v[176:177], v[6:7], v[172:173]
	v_pk_mul_f32 v[172:173], v[180:181], v[178:179] op_sel_hi:[0,1]
	v_pk_mul_f32 v[166:167], v[180:181], v[166:167] op_sel_hi:[0,1]
	v_pk_mul_f32 v[178:179], v[180:181], v[194:195] op_sel_hi:[0,1]
	v_pk_mul_f32 v[174:175], v[180:181], v[196:197] op_sel_hi:[0,1]
	v_max_f32_e64 v180, |v170|, |v171|
	v_max_f32_e64 v181, |v164|, |v165|
	v_pk_mul_f32 v[166:167], v[12:13], v[166:167]
	v_pk_mul_f32 v[172:173], v[10:11], v[172:173]
	v_max3_f32 v180, v180, 0, v181
	v_max_f32_e64 v181, |v176|, |v177|
	v_max_f32_e64 v194, |v168|, |v169|
	v_pk_mul_f32 v[174:175], v[16:17], v[174:175]
	v_pk_mul_f32 v[178:179], v[14:15], v[178:179]
	v_max3_f32 v180, v180, v181, v194
	v_max_f32_e64 v181, |v172|, |v173|
	v_max_f32_e64 v194, |v166|, |v167|
	v_max3_f32 v180, v180, v181, v194
	v_max_f32_e64 v181, |v178|, |v179|
	v_max_f32_e64 v194, |v174|, |v175|
	v_max3_f32 v180, v180, v181, v194
	s_nop 1
	v_max_f32_dpp v180, v180, v180 quad_perm:[1,0,3,2] row_mask:0xf bank_mask:0xf
	s_nop 1
	v_max_f32_dpp v180, v180, v180 quad_perm:[2,3,0,1] row_mask:0xf bank_mask:0xf
	s_nop 1
	v_max_f32_dpp v180, v180, v180 row_half_mirror row_mask:0xf bank_mask:0xf
	s_nop 1
	v_max_f32_dpp v180, v180, v180 row_ror:8 row_mask:0xf bank_mask:0xf
	v_mov_b32_e32 v181, v180
	s_nop 1
	v_permlane16_swap_b32_e32 v180, v181
	s_nop 0
	v_max_f32_e32 v180, v180, v181
	v_mov_b32_e32 v181, v180
	s_nop 1
	v_permlane32_swap_b32_e32 v180, v181
	s_nop 0
	v_max_f32_e32 v180, v180, v181
	s_and_saveexec_b64 s[4:5], s[10:11]
	s_xor_b64 s[18:19], exec, s[4:5]
	s_add_u32 s20, s50, s36
	s_addc_u32 s21, s51, s37
	s_or_saveexec_b64 s[18:19], s[18:19]
	s_waitcnt lgkmcnt(0)
	v_max_f32_e32 v204, s72, v180
	v_mov_b64_e32 v[180:181], s[20:21]
	s_xor_b64 exec, exec, s[18:19]
	s_cbranch_execz .LBB0_955
	s_ashr_i32 s41, s40, 31
	s_add_u32 s4, s6, s38
	v_mul_f32_e32 v180, 0x3c010204, v204
	s_addc_u32 s5, s7, s39
	global_store_dword v1, v180, s[4:5]
	v_mov_b64_e32 v[180:181], s[40:41]
.LBB0_955:
	s_or_b64 exec, exec, s[18:19]
	v_div_scale_f32 v194, s[4:5], v204, v204, s73
	v_rcp_f32_e32 v195, v194
	v_lshlrev_b64 v[180:181], 10, v[180:181]
	v_lshl_add_u64 v[180:181], v[150:151], 0, v[180:181]
	s_mov_b32 s4, 0xff61b1e6
	v_fma_f32 v196, -v194, v195, 1.0
	v_fmac_f32_e32 v195, v196, v195
	v_div_scale_f32 v196, vcc, s73, v204, s73
	v_mul_f32_e32 v197, v196, v195
	v_fma_f32 v205, -v194, v197, v196
	v_fmac_f32_e32 v197, v205, v195
	v_fma_f32 v194, -v194, v197, v196
	v_div_fmas_f32 v194, v194, v195, v197
	v_div_fixup_f32 v194, v194, v204, s73
	v_mul_f32_e32 v196, v171, v194
	v_mul_f32_e32 v197, v164, v194
	v_mul_f32_e32 v195, v170, v194
	v_mul_f32_e32 v204, v165, v194
	v_rndne_f32_e32 v196, v196
	v_rndne_f32_e32 v197, v197
	v_rndne_f32_e32 v195, v195
	v_cvt_i32_f32_e32 v196, v196
	v_cvt_i32_f32_e32 v197, v197
	v_rndne_f32_e32 v204, v204
	v_cvt_i32_f32_e32 v195, v195
	v_cvt_i32_f32_e32 v204, v204
	v_med3_i32 v196, v196, s84, v236
	v_med3_i32 v197, v197, s84, v236
	v_med3_i32 v195, v195, s84, v236
	v_med3_i32 v204, v204, s84, v236
	v_lshlrev_b32_e32 v196, 8, v196
	v_lshlrev_b32_e32 v197, 16, v197
	v_and_b32_e32 v196, 0xff00, v196
	v_and_b32_e32 v197, 0xff0000, v197
	v_perm_b32 v195, v204, v195, s60
	v_or3_b32 v195, v195, v196, v197
	v_mul_f32_e32 v196, v177, v194
	v_mul_f32_e32 v197, v168, v194
	global_store_dword v[180:181], v195, off
	v_mul_f32_e32 v195, v176, v194
	v_mul_f32_e32 v204, v169, v194
	v_rndne_f32_e32 v196, v196
	v_rndne_f32_e32 v197, v197
	v_rndne_f32_e32 v195, v195
	v_cvt_i32_f32_e32 v196, v196
	v_cvt_i32_f32_e32 v197, v197
	v_rndne_f32_e32 v204, v204
	v_cvt_i32_f32_e32 v195, v195
	v_cvt_i32_f32_e32 v204, v204
	v_med3_i32 v196, v196, s84, v236
	v_med3_i32 v197, v197, s84, v236
	v_med3_i32 v195, v195, s84, v236
	v_med3_i32 v204, v204, s84, v236
	v_lshlrev_b32_e32 v196, 8, v196
	v_lshlrev_b32_e32 v197, 16, v197
	v_and_b32_e32 v196, 0xff00, v196
	v_and_b32_e32 v197, 0xff0000, v197
	v_perm_b32 v195, v204, v195, s60
	v_or3_b32 v195, v195, v196, v197
	v_mul_f32_e32 v196, v173, v194
	v_mul_f32_e32 v197, v166, v194
	global_store_dword v[180:181], v195, off offset:256
	v_mul_f32_e32 v195, v172, v194
	v_mul_f32_e32 v204, v167, v194
	v_rndne_f32_e32 v196, v196
	v_rndne_f32_e32 v197, v197
	v_rndne_f32_e32 v195, v195
	v_cvt_i32_f32_e32 v196, v196
	v_cvt_i32_f32_e32 v197, v197
	v_rndne_f32_e32 v204, v204
	v_cvt_i32_f32_e32 v195, v195
	v_cvt_i32_f32_e32 v204, v204
	v_med3_i32 v196, v196, s84, v236
	v_med3_i32 v197, v197, s84, v236
	v_med3_i32 v195, v195, s84, v236
	v_med3_i32 v204, v204, s84, v236
	v_lshlrev_b32_e32 v196, 8, v196
	v_lshlrev_b32_e32 v197, 16, v197
	v_and_b32_e32 v196, 0xff00, v196
	v_and_b32_e32 v197, 0xff0000, v197
	v_perm_b32 v195, v204, v195, s60
	v_or3_b32 v195, v195, v196, v197
	v_mul_f32_e32 v196, v179, v194
	v_mul_f32_e32 v197, v174, v194
	global_store_dword v[180:181], v195, off offset:512
	v_mul_f32_e32 v195, v178, v194
	v_mul_f32_e32 v194, v175, v194
	v_rndne_f32_e32 v196, v196
	v_rndne_f32_e32 v197, v197
	v_rndne_f32_e32 v195, v195
	v_cvt_i32_f32_e32 v196, v196
	v_cvt_i32_f32_e32 v197, v197
	v_rndne_f32_e32 v194, v194
	v_cvt_i32_f32_e32 v195, v195
	v_cvt_i32_f32_e32 v194, v194
	v_med3_i32 v196, v196, s84, v236
	v_med3_i32 v197, v197, s84, v236
	v_med3_i32 v195, v195, s84, v236
	v_med3_i32 v194, v194, s84, v236
	v_lshlrev_b32_e32 v196, 8, v196
	v_lshlrev_b32_e32 v197, 16, v197
	v_and_b32_e32 v196, 0xff00, v196
	v_and_b32_e32 v197, 0xff0000, v197
	v_perm_b32 v194, v194, v195, s60
	v_or3_b32 v194, v194, v196, v197
	global_store_dword v[180:181], v194, off offset:768
	v_fma_f32 v180, v30, v170, 0
	v_fma_f32 v196, v26, v170, 0
	v_fmac_f32_e32 v180, v22, v171
	v_fma_f32 v181, v31, v170, 0
	v_fmac_f32_e32 v196, v18, v171
	v_fma_f32 v197, v27, v170, 0
	v_fmac_f32_e32 v180, v46, v164
	v_fmac_f32_e32 v181, v23, v171
	v_fma_f32 v194, v32, v170, 0
	v_fmac_f32_e32 v196, v42, v164
	v_fmac_f32_e32 v197, v19, v171
	v_fma_f32 v204, v28, v170, 0
	v_fmac_f32_e32 v180, v38, v165
	v_fmac_f32_e32 v181, v47, v164
	v_fmac_f32_e32 v194, v24, v171
	v_fma_f32 v195, v33, v170, 0
	v_fmac_f32_e32 v196, v34, v165
	v_fmac_f32_e32 v197, v43, v164
	v_fmac_f32_e32 v204, v20, v171
	v_fma_f32 v170, v29, v170, 0
	v_fmac_f32_e32 v180, v50, v176
	v_fmac_f32_e32 v181, v39, v165
	v_fmac_f32_e32 v194, v48, v164
	v_fmac_f32_e32 v195, v25, v171
	v_fmac_f32_e32 v196, v62, v176
	v_fmac_f32_e32 v197, v35, v165
	v_fmac_f32_e32 v204, v44, v164
	v_fmac_f32_e32 v170, v21, v171
	v_fmac_f32_e32 v180, v58, v177
	v_fmac_f32_e32 v181, v51, v176
	v_fmac_f32_e32 v194, v40, v165
	v_fmac_f32_e32 v195, v49, v164
	v_fmac_f32_e32 v196, v54, v177
	v_fmac_f32_e32 v197, v63, v176
	v_fmac_f32_e32 v204, v36, v165
	v_fmac_f32_e32 v170, v45, v164
	v_fmac_f32_e32 v180, v74, v168
	v_fmac_f32_e32 v181, v59, v177
	v_fmac_f32_e32 v194, v52, v176
	v_fmac_f32_e32 v195, v41, v165
	v_fmac_f32_e32 v196, v78, v168
	v_fmac_f32_e32 v197, v55, v177
	v_fmac_f32_e32 v204, v64, v176
	v_fmac_f32_e32 v170, v37, v165
	v_fmac_f32_e32 v180, v70, v169
	v_fmac_f32_e32 v181, v75, v168
	v_fmac_f32_e32 v194, v60, v177
	v_fmac_f32_e32 v195, v53, v176
	v_fmac_f32_e32 v196, v66, v169
	v_fmac_f32_e32 v197, v79, v168
	v_fmac_f32_e32 v204, v56, v177
	v_fmac_f32_e32 v170, v65, v176
	v_fmac_f32_e32 v180, v82, v172
	v_fmac_f32_e32 v181, v71, v169
	v_fmac_f32_e32 v194, v76, v168
	v_fmac_f32_e32 v195, v61, v177
	v_fmac_f32_e32 v196, v94, v172
	v_fmac_f32_e32 v197, v67, v169
	v_fmac_f32_e32 v204, v80, v168
	v_fmac_f32_e32 v170, v57, v177
	v_fmac_f32_e32 v180, v90, v173
	v_fmac_f32_e32 v181, v83, v172
	v_fmac_f32_e32 v194, v72, v169
	v_fmac_f32_e32 v195, v77, v168
	v_fmac_f32_e32 v196, v86, v173
	v_fmac_f32_e32 v197, v95, v172
	v_fmac_f32_e32 v204, v68, v169
	v_fmac_f32_e32 v170, v81, v168
	v_fmac_f32_e32 v180, v106, v166
	v_fmac_f32_e32 v181, v91, v173
	v_fmac_f32_e32 v194, v84, v172
	v_fmac_f32_e32 v195, v73, v169
	v_fmac_f32_e32 v196, v110, v166
	v_fmac_f32_e32 v197, v87, v173
	v_fmac_f32_e32 v204, v96, v172
	v_fmac_f32_e32 v170, v69, v169
	v_fmac_f32_e32 v180, v102, v167
	v_fmac_f32_e32 v181, v107, v166
	v_fmac_f32_e32 v194, v92, v173
	v_fmac_f32_e32 v195, v85, v172
	v_fmac_f32_e32 v196, v98, v167
	v_fmac_f32_e32 v197, v111, v166
	v_fmac_f32_e32 v204, v88, v173
	v_fmac_f32_e32 v170, v97, v172
	v_fmac_f32_e32 v180, v114, v178
	v_fmac_f32_e32 v181, v103, v167
	v_fmac_f32_e32 v194, v108, v166
	v_fmac_f32_e32 v195, v93, v173
	v_fmac_f32_e32 v196, v126, v178
	v_fmac_f32_e32 v197, v99, v167
	v_fmac_f32_e32 v204, v112, v166
	v_fmac_f32_e32 v170, v89, v173
	v_fmac_f32_e32 v180, v122, v179
	v_fmac_f32_e32 v181, v115, v178
	v_fmac_f32_e32 v194, v104, v167
	v_fmac_f32_e32 v195, v109, v166
	v_fmac_f32_e32 v196, v118, v179
	v_fmac_f32_e32 v197, v127, v178
	v_fmac_f32_e32 v204, v100, v167
	v_fmac_f32_e32 v170, v113, v166
	v_fmac_f32_e32 v180, v138, v174
	v_fmac_f32_e32 v181, v123, v179
	v_fmac_f32_e32 v194, v116, v178
	v_fmac_f32_e32 v195, v105, v167
	v_fmac_f32_e32 v196, v142, v174
	v_fmac_f32_e32 v197, v119, v179
	v_fmac_f32_e32 v204, v128, v178
	v_fmac_f32_e32 v170, v101, v167
	v_fmac_f32_e32 v180, v134, v175
	v_fmac_f32_e32 v181, v139, v174
	v_fmac_f32_e32 v194, v124, v179
	v_fmac_f32_e32 v195, v117, v178
	v_fmac_f32_e32 v196, v130, v175
	v_fmac_f32_e32 v197, v143, v174
	v_fmac_f32_e32 v204, v120, v179
	v_fmac_f32_e32 v170, v129, v178
	v_fmac_f32_e32 v181, v135, v175
	v_fmac_f32_e32 v194, v140, v174
	v_fmac_f32_e32 v195, v125, v179
	v_fmac_f32_e32 v197, v131, v175
	v_fmac_f32_e32 v204, v144, v174
	v_fmac_f32_e32 v170, v121, v179
	v_cndmask_b32_e64 v165, v180, v196, s[12:13]
	v_fmac_f32_e32 v194, v136, v175
	v_fmac_f32_e32 v195, v141, v174
	v_fmac_f32_e32 v204, v132, v175
	v_fmac_f32_e32 v170, v145, v174
	v_cndmask_b32_e64 v166, v181, v197, s[12:13]
	v_fmac_f32_e32 v195, v137, v175
	v_fmac_f32_e32 v170, v133, v175
	v_cndmask_b32_e64 v167, v194, v204, s[12:13]
	v_cndmask_b32_e64 v168, v195, v170, s[12:13]
	v_cndmask_b32_e64 v164, v196, v180, s[12:13]
	s_nop 1
	v_add_f32_dpp v164, v165, v164 row_shl:4 row_mask:0xf bank_mask:0x5
	s_nop 1
	v_add_f32_dpp v164, v165, v164 row_shr:4 row_mask:0xf bank_mask:0xa
	v_cndmask_b32_e64 v165, v197, v181, s[12:13]
	s_nop 1
	v_add_f32_dpp v165, v166, v165 row_shl:4 row_mask:0xf bank_mask:0x5
	s_nop 1
	v_add_f32_dpp v165, v166, v165 row_shr:4 row_mask:0xf bank_mask:0xa
	v_cndmask_b32_e64 v166, v204, v194, s[12:13]
	s_nop 1
	v_add_f32_dpp v166, v167, v166 row_shl:4 row_mask:0xf bank_mask:0x5
	s_nop 1
	v_add_f32_dpp v166, v167, v166 row_shr:4 row_mask:0xf bank_mask:0xa
	v_cndmask_b32_e64 v167, v170, v195, s[12:13]
	s_nop 1
	v_add_f32_dpp v167, v168, v167 row_shl:4 row_mask:0xf bank_mask:0x5
	s_nop 1
	v_add_f32_dpp v167, v168, v167 row_shr:4 row_mask:0xf bank_mask:0xa
	v_cndmask_b32_e64 v168, v166, v164, s[14:15]
	v_cndmask_b32_e64 v164, v164, v166, s[14:15]
	v_cndmask_b32_e64 v166, v167, v165, s[14:15]
	v_cndmask_b32_e64 v165, v165, v167, s[14:15]
	v_mov_b32_e32 v175, 0xff61b1e6
	s_nop 1
	v_add_f32_dpp v164, v164, v168 quad_perm:[2,3,0,1] row_mask:0xf bank_mask:0xf
	v_add_f32_dpp v165, v165, v166 quad_perm:[2,3,0,1] row_mask:0xf bank_mask:0xf
	v_cndmask_b32_e64 v166, v165, v164, s[16:17]
	v_cndmask_b32_e64 v164, v164, v165, s[16:17]
	s_nop 1
	v_add_f32_dpp v164, v164, v166 quad_perm:[1,0,3,2] row_mask:0xf bank_mask:0xf
	s_nop 1
	v_add_f32_dpp v164, v164, v164 row_ror:8 row_mask:0xf bank_mask:0xf
	v_mov_b32_e32 v165, v164
	s_nop 1
	v_permlane16_swap_b32_e32 v164, v165
	s_nop 0
	v_add_f32_e32 v164, v164, v165
	v_mov_b32_e32 v165, v164
	s_nop 1
	v_permlane32_swap_b32_e32 v164, v165
	s_nop 0
	v_add_f32_e32 v164, v164, v165
	ds_bpermute_b32 v166, v191, v164
	ds_bpermute_b32 v168, v192, v164
	ds_bpermute_b32 v169, v193, v164
	ds_bpermute_b32 v170, v198, v164
	ds_bpermute_b32 v171, v199, v164
	ds_bpermute_b32 v172, v200, v164
	s_waitcnt lgkmcnt(4)
	v_cmp_gt_f32_e32 vcc, v168, v166
	ds_bpermute_b32 v173, v201, v164
	ds_bpermute_b32 v165, v202, v164
	v_cndmask_b32_e32 v167, v166, v168, vcc
	v_cndmask_b32_e64 v164, 0, 1, vcc
	s_waitcnt lgkmcnt(5)
	v_cmp_lt_f32_e32 vcc, v167, v169
	v_cmp_nlt_f32_e64 s[24:25], s4, v166
	s_nop 0
	v_cndmask_b32_e32 v167, v167, v169, vcc
	v_cndmask_b32_e64 v164, v164, 2, vcc
	s_waitcnt lgkmcnt(4)
	v_cmp_lt_f32_e32 vcc, v167, v170
	s_nop 1
	v_cndmask_b32_e32 v167, v167, v170, vcc
	v_cndmask_b32_e64 v164, v164, 3, vcc
	s_waitcnt lgkmcnt(3)
	v_cmp_lt_f32_e32 vcc, v167, v171
	s_nop 1
	v_cndmask_b32_e32 v167, v167, v171, vcc
	v_cndmask_b32_e64 v164, v164, 4, vcc
	s_waitcnt lgkmcnt(2)
	v_cmp_lt_f32_e32 vcc, v167, v172
	s_nop 1
	v_cndmask_b32_e32 v167, v167, v172, vcc
	v_cndmask_b32_e64 v164, v164, 5, vcc
	s_waitcnt lgkmcnt(1)
	v_cmp_nlt_f32_e32 vcc, v167, v173
	s_nop 1
	v_cndmask_b32_e32 v167, v173, v167, vcc
	v_cndmask_b32_e32 v164, 6, v164, vcc
	s_waitcnt lgkmcnt(0)
	v_cmp_lt_f32_e64 s[20:21], v167, v165
	s_or_b64 s[4:5], vcc, s[20:21]
	v_cmp_nlt_f32_e64 s[18:19], v167, v165
	v_cndmask_b32_e64 v164, v164, 7, s[20:21]
	v_cmp_eq_u32_e64 s[22:23], 0, v164
	s_or_b64 s[22:23], s[24:25], s[22:23]
	s_nop 0
	v_cndmask_b32_e64 v166, v166, v175, s[22:23]
	v_cndmask_b32_e64 v174, 0, -1, s[22:23]
	v_cmp_ne_u32_e64 s[22:23], 1, v164
	v_cmp_lt_f32_e64 s[24:25], v166, v168
	s_and_b64 s[22:23], s[22:23], s[24:25]
	v_cndmask_b32_e64 v166, v166, v168, s[22:23]
	v_cndmask_b32_e64 v174, v174, 1, s[22:23]
	v_cmp_ne_u32_e64 s[22:23], 2, v164
	v_cmp_lt_f32_e64 s[24:25], v166, v169
	s_and_b64 s[22:23], s[22:23], s[24:25]
	v_cndmask_b32_e64 v166, v166, v169, s[22:23]
	v_cndmask_b32_e64 v168, v174, 2, s[22:23]
	v_cmp_ne_u32_e64 s[22:23], 3, v164
	v_cmp_lt_f32_e64 s[24:25], v166, v170
	s_and_b64 s[22:23], s[22:23], s[24:25]
	v_cndmask_b32_e64 v166, v166, v170, s[22:23]
	v_cndmask_b32_e64 v168, v168, 3, s[22:23]
	v_cmp_ne_u32_e64 s[22:23], 4, v164
	v_cmp_lt_f32_e64 s[24:25], v166, v171
	s_and_b64 s[22:23], s[22:23], s[24:25]
	v_cndmask_b32_e64 v166, v166, v171, s[22:23]
	v_cndmask_b32_e64 v168, v168, 4, s[22:23]
	v_cmp_ne_u32_e64 s[22:23], 5, v164
	v_cmp_lt_f32_e64 s[24:25], v166, v172
	s_and_b64 s[22:23], s[22:23], s[24:25]
	v_cndmask_b32_e64 v169, v166, v172, s[22:23]
	v_cmp_lt_f32_e32 vcc, v169, v173
	v_cndmask_b32_e64 v168, v168, 5, s[22:23]
	s_and_b64 vcc, s[4:5], vcc
	v_cndmask_b32_e64 v166, v168, 6, vcc
	v_cndmask_b32_e32 v168, v169, v173, vcc
	s_and_saveexec_b64 s[20:21], s[18:19]
	s_cbranch_execz .LBB0_959
	v_cmp_lt_f32_e32 vcc, v168, v165
	s_and_saveexec_b64 s[18:19], vcc
	v_mov_b32_e32 v166, 7
	v_mov_b32_e32 v168, v165
	s_or_b64 exec, exec, s[18:19]
	v_mov_b32_e32 v165, v167

.LBB0_1022:
	v_lshlrev_b32_e32 v39, 16, v37
	v_lshlrev_b32_e32 v38, 16, v36
	v_and_b32_e32 v37, 0xffff0000, v37
	v_and_b32_e32 v36, 0xffff0000, v36
	v_lshlrev_b32_e32 v41, 16, v35
	v_lshlrev_b32_e32 v40, 16, v34
	v_and_b32_e32 v35, 0xffff0000, v35
	v_and_b32_e32 v34, 0xffff0000, v34
	v_lshlrev_b32_e32 v46, 16, v32
	v_and_b32_e32 v47, 0xffff0000, v32
	v_lshlrev_b32_e32 v32, 16, v33
	v_lshlrev_b32_e32 v54, 16, v30
	v_pk_mul_f32 v[42:43], v[36:37], v[36:37]
	v_pk_mul_f32 v[44:45], v[34:35], v[34:35]
	v_and_b32_e32 v33, 0xffff0000, v33
	v_pk_fma_f32 v[42:43], v[38:39], v[38:39], v[42:43]
	v_pk_fma_f32 v[44:45], v[40:41], v[40:41], v[44:45]
	v_mul_f32_e32 v55, v46, v46
	v_mul_f32_e32 v57, v47, v47
	v_mul_f32_e32 v0, v32, v32
	v_mov_b32_e32 v56, v54
	v_and_b32_e32 v62, 0xffff0000, v30
	v_lshlrev_b32_e32 v30, 16, v31
	v_and_b32_e32 v31, 0xffff0000, v31
	v_pk_add_f32 v[42:43], v[42:43], v[42:43] op_sel_hi:[0,1]
	v_pk_add_f32 v[44:45], v[44:45], v[44:45] op_sel_hi:[0,1]
	v_pk_fma_f32 v[58:59], v[32:33], v[32:33], v[0:1] op_sel_hi:[1,1,0]
	v_pk_add_f32 v[56:57], v[54:55], v[56:57]
	v_mul_f32_e32 v58, v62, v62
	v_mul_f32_e32 v42, v30, v30
	v_mul_f32_e32 v44, v31, v31
	v_mul_f32_e32 v60, v54, v54
	v_mov_b32_e32 v61, v57
	v_pk_add_f32 v[56:57], v[60:61], v[58:59]
	v_pk_add_f32 v[42:43], v[42:43], v[44:45]
	v_mov_b32_e32 v55, v62
	v_pk_add_f32 v[42:43], v[56:57], v[42:43]
	s_nop 0
	v_add_f32_e32 v0, v42, v43
	v_mov_b32_e32 v43, v36
	v_mov_b32_e32 v36, v39
	v_add_f32_dpp v0, v0, v0 quad_perm:[1,0,3,2] row_mask:0xf bank_mask:0xf
	s_nop 1
	v_add_f32_dpp v0, v0, v0 quad_perm:[2,3,0,1] row_mask:0xf bank_mask:0xf
	s_nop 1
	v_add_f32_dpp v0, v0, v0 row_half_mirror row_mask:0xf bank_mask:0xf
	s_nop 1
	v_add_f32_dpp v0, v0, v0 row_ror:8 row_mask:0xf bank_mask:0xf
	v_mov_b32_e32 v42, v0
	s_nop 1
	v_permlane16_swap_b32_e32 v0, v42
	s_nop 0
	v_add_f32_e32 v0, v0, v42
	v_mov_b32_e32 v42, v0
	s_nop 1
	v_permlane32_swap_b32_e32 v0, v42
	s_nop 0
	v_add_f32_e32 v0, v0, v42
	v_fmamk_f32 v0, v0, 0x3a800000, v235
	v_rsq_f32_e32 v0, v0
	v_mov_b32_e32 v42, v38
	v_pk_mul_f32 v[36:37], v[0:1], v[36:37] op_sel_hi:[0,1]
	v_pk_mul_f32 v[44:45], v[0:1], v[42:43] op_sel_hi:[0,1]
	v_pk_mul_f32 v[42:43], v[16:17], v[36:37]
	v_mov_b32_e32 v36, v40
	v_mov_b32_e32 v37, v34
	v_mov_b32_e32 v34, v41
	v_pk_mul_f32 v[44:45], v[14:15], v[44:45]
	v_pk_mul_f32 v[36:37], v[0:1], v[36:37] op_sel_hi:[0,1]
	v_pk_mul_f32 v[34:35], v[0:1], v[34:35] op_sel_hi:[0,1]
	v_pk_mul_f32 v[32:33], v[32:33], v[0:1] op_sel_hi:[1,0]
	v_pk_mul_f32 v[38:39], v[12:13], v[34:35]
	v_pk_mul_f32 v[40:41], v[10:11], v[36:37]
	v_pk_mul_f32 v[36:37], v[46:47], v[0:1] op_sel_hi:[1,0]
	v_pk_mul_f32 v[34:35], v[8:9], v[32:33]
	v_pk_mul_f32 v[32:33], v[54:55], v[0:1] op_sel_hi:[1,0]
	v_pk_mul_f32 v[30:31], v[30:31], v[0:1] op_sel_hi:[1,0]
	v_max_f32_e64 v0, |v44|, |v45|
	v_max_f32_e64 v46, |v42|, |v43|
	v_pk_mul_f32 v[36:37], v[6:7], v[36:37]
	v_max3_f32 v0, v0, 0, v46
	v_max_f32_e64 v46, |v40|, |v41|
	v_max_f32_e64 v47, |v38|, |v39|
	v_pk_mul_f32 v[30:31], v[4:5], v[30:31]
	v_pk_mul_f32 v[32:33], v[2:3], v[32:33]
	v_max3_f32 v0, v0, v46, v47
	v_max_f32_e64 v46, |v36|, |v37|
	v_max_f32_e64 v47, |v34|, |v35|
	v_max3_f32 v0, v0, v46, v47
	v_max_f32_e64 v46, |v32|, |v33|
	v_max_f32_e64 v47, |v30|, |v31|
	v_max3_f32 v0, v0, v46, v47
	s_nop 1
	v_max_f32_dpp v0, v0, v0 quad_perm:[1,0,3,2] row_mask:0xf bank_mask:0xf
	s_nop 1
	v_max_f32_dpp v0, v0, v0 quad_perm:[2,3,0,1] row_mask:0xf bank_mask:0xf
	s_nop 1
	v_max_f32_dpp v0, v0, v0 row_half_mirror row_mask:0xf bank_mask:0xf
	s_nop 1
	v_max_f32_dpp v0, v0, v0 row_ror:8 row_mask:0xf bank_mask:0xf
	v_mov_b32_e32 v46, v0
	s_nop 1
	v_permlane16_swap_b32_e32 v0, v46
	s_nop 0
	v_max_f32_e32 v0, v0, v46
	v_mov_b32_e32 v46, v0
	s_nop 1
	v_permlane32_swap_b32_e32 v0, v46
	s_nop 0
	v_max_f32_e32 v0, v0, v46
	v_max_f32_e32 v0, s72, v0
	v_mov_b64_e32 v[46:47], s[12:13]
	s_and_saveexec_b64 s[14:15], s[8:9]
	s_cbranch_execz .LBB0_1018
	s_bfe_i64 s[4:5], s[12:13], 0x200000
	s_add_u32 s16, s6, s10
	v_mul_f32_e32 v46, 0x3c010204, v0
	s_addc_u32 s17, s7, s11
	global_store_dword v1, v46, s[16:17]
	v_mov_b64_e32 v[46:47], s[4:5]
	s_branch .LBB0_1018
